# HGRN2 chunk loop: row addresses of the 32 per-chunk loads kept as 32-bit offsets against a uniform base (saddr), 92 address VALU ops per chunk replaced by 16 adds
# baseline (speedup 1.0000x reference)
; __device__ __forceinline__ void hgrn_mfma(const Params& p, LAS unsigned char* lds) {
;     ...
;         const int b = u >> 4, h = (u >> 1) & 7, dir = u & 1;
;         const int d = 16 * w + fr;
;         float lb; { const float l0 = lbl[h * 128 + d], l1 = lbl[1024 + h * 128 + d], l2 = lbl[2048 + h * 128 + d];
;             const float mx = fmaxf(l0, fmaxf(l1, l2)); const float e0 = expf(l0 - mx), e1 = expf(l1 - mx), e2 = expf(l2 - mx); lb = e0 / (e0 + e1 + e2); }
;         f32x4 S[8];
; #pragma unroll
;         for (int mi = 0; mi < 8; ++mi) S[mi] = (f32x4){0.f, 0.f, 0.f, 0.f};
;         const bf16_t* pb = proj + (size_t)b * T * LD0 + h * 128 + d;
;         const int zoff = dir ? 3072 : 2048;
;         bf16_t rq[8], rz[8], rv[8], rp[8];
;     ...
;         HG_LOAD(0);
.LBB0_274:
	s_lshl_b32 s18, s53, 6
	s_and_b32 s18, s18, 0x380
	v_add_u32_e32 v2, s18, v38
	v_ashrrev_i32_e32 v3, 31, v2
	s_waitcnt lgkmcnt(0)
	v_lshl_add_u64 v[2:3], v[2:3], 2, s[40:41]
	v_add_co_u32_e32 v6, vcc, 0x1000, v2
	s_ashr_i32 s46, s53, 4
	s_nop 0
	v_addc_co_u32_e32 v7, vcc, 0, v3, vcc
	v_add_co_u32_e32 v8, vcc, 0x2000, v2
	s_and_b32 s54, s53, 1
	s_nop 0
	v_addc_co_u32_e32 v9, vcc, 0, v3, vcc
	global_load_dword v0, v[2:3], off
	global_load_dword v16, v[6:7], off
	global_load_dword v17, v[8:9], off
	s_ashr_i32 s47, s46, 31
	s_mul_i32 s42, s46, 0x2040000
	s_mul_hi_i32 s19, s46, 0x2040000
	s_add_u32 s42, s36, s42
	s_addc_u32 s19, s37, s19
	s_lshl_b32 s56, s18, 1
	s_add_u32 s18, s42, s56
	s_addc_u32 s19, s19, 0
	s_cmp_eq_u32 s54, 0
	v_lshl_add_u64 v[44:45], v[38:39], 1, s[18:19]
	s_cselect_b64 s[18:19], -1, 0
	v_cndmask_b32_e64 v2, v66, v41, s[18:19]
	v_cndmask_b32_e64 v5, v67, v40, s[18:19]
	v_cndmask_b32_e64 v8, v69, v68, s[18:19]
	s_and_b64 s[58:59], s[18:19], exec
	v_mul_u32_u24_e32 v2, 0x2040, v2
	v_mul_u32_u24_e32 v6, 0x4080, v5
	v_mul_u32_u24_e32 v5, 0x2040, v8
	v_mov_b32_e32 v3, v4
	v_mov_b32_e32 v9, v4
	v_cndmask_b32_e64 v10, v71, v70, s[18:19]
	s_cselect_b32 s55, s50, 0xc00
	v_lshlrev_b32_e32 v2, 1, v2
	v_lshlrev_b32_e32 v8, 1, v5
	v_mov_b32_e32 v7, v4
	v_mov_b32_e32 v11, v4
	v_mul_u32_u24_e32 v10, 0x4080, v10
	v_lshl_add_u64 v[2:3], v[44:45], 0, v[2:3]
	s_lshl_b32 s42, s55, 1
	v_lshl_add_u64 v[8:9], v[44:45], 0, v[8:9]
	v_lshl_add_u64 v[6:7], v[44:45], 0, v[6:7]
	v_lshl_add_u64 v[10:11], v[44:45], 0, v[10:11]
	v_lshl_add_u64 v[12:13], v[2:3], 0, s[42:43]
	v_lshl_add_u64 v[14:15], v[8:9], 0, s[42:43]
	global_load_ushort v135, v[2:3], off
	global_load_ushort v159, v[2:3], off offset:2048
	global_load_ushort v137, v[12:13], off
	global_load_ushort v171, v[6:7], off offset:2048
	global_load_ushort v136, v[8:9], off
	global_load_ushort v160, v[8:9], off offset:2048
	global_load_ushort v138, v[14:15], off
	global_load_ushort v5, v[10:11], off offset:2048
	v_cndmask_b32_e64 v18, v73, v72, s[18:19]
	v_cndmask_b32_e64 v14, v79, v78, s[18:19]
	v_mul_u32_u24_e32 v14, 0x4080, v14
	v_mov_b32_e32 v15, v4
	v_lshl_add_u64 v[14:15], v[44:45], 0, v[14:15]
	s_lshl_b64 s[46:47], s[46:47], 22
	v_mov_b32_e32 v21, v4
	v_mov_b32_e32 v22, v4
	v_mov_b32_e32 v23, v4
	v_mov_b32_e32 v24, v4
	v_mov_b32_e32 v25, v4
	v_mov_b32_e32 v26, v4
	v_mov_b32_e32 v27, v4
	v_mov_b32_e32 v28, v4
	v_mov_b32_e32 v29, v4
	v_mov_b32_e32 v30, v4
	v_mov_b32_e32 v31, v4
	v_mov_b32_e32 v32, v4
	v_mov_b32_e32 v33, v4
	v_mov_b32_e32 v34, v4
	v_mov_b32_e32 v35, v4
	v_mov_b32_e32 v36, v4
	v_mov_b32_e32 v37, v4
	s_waitcnt vmcnt(8)
	v_max3_f32 v2, v0, v16, v17
	v_sub_f32_e32 v0, v0, v2
	v_sub_f32_e32 v3, v16, v2
	v_sub_f32_e32 v16, v17, v2
	v_mul_f32_e32 v2, 0x3fb8aa3b, v0
	v_mul_f32_e32 v6, 0x3fb8aa3b, v3
	v_fma_f32 v8, v0, s3, -v2
	v_rndne_f32_e32 v9, v2
	v_fma_f32 v10, v3, s3, -v6
	v_rndne_f32_e32 v11, v6
	v_fmac_f32_e32 v8, 0x32a5705f, v0
	v_sub_f32_e32 v2, v2, v9
	v_fmac_f32_e32 v10, 0x32a5705f, v3
	v_sub_f32_e32 v6, v6, v11
	v_add_f32_e32 v2, v2, v8
	v_cvt_i32_f32_e32 v9, v9
	v_add_f32_e32 v6, v6, v10
	v_exp_f32_e32 v2, v2
	v_cvt_i32_f32_e32 v11, v11
	v_exp_f32_e32 v6, v6
	v_cmp_ngt_f32_e32 vcc, s48, v0
	v_ldexp_f32 v2, v2, v9
	v_mul_f32_e32 v7, 0x3fb8aa3b, v16
	v_ldexp_f32 v6, v6, v11
	v_cndmask_b32_e32 v2, 0, v2, vcc
	v_cmp_ngt_f32_e32 vcc, s48, v3
	v_cndmask_b32_e64 v10, v77, v76, s[18:19]
	v_fma_f32 v12, v16, s3, -v7
	v_cndmask_b32_e32 v6, 0, v6, vcc
	v_cmp_nlt_f32_e32 vcc, s49, v0
	v_rndne_f32_e32 v13, v7
	v_mul_u32_u24_e32 v10, 0x2040, v10
	v_cndmask_b32_e32 v0, v134, v2, vcc
	v_mul_u32_u24_e32 v2, 0x2040, v18
	v_fmac_f32_e32 v12, 0x32a5705f, v16
	v_sub_f32_e32 v7, v7, v13
	v_cmp_nlt_f32_e32 vcc, s49, v3
	v_lshlrev_b32_e32 v2, 1, v2
	v_mov_b32_e32 v3, v4
	v_cndmask_b32_e64 v8, v75, v74, s[18:19]
	v_lshlrev_b32_e32 v10, 1, v10
	v_mov_b32_e32 v11, v4
	v_add_f32_e32 v7, v7, v12
	v_lshl_add_u64 v[2:3], v[44:45], 0, v[2:3]
	v_mul_u32_u24_e32 v8, 0x4080, v8
	v_mov_b32_e32 v9, v4
	v_lshl_add_u64 v[10:11], v[44:45], 0, v[10:11]
	v_cvt_i32_f32_e32 v17, v13
	v_exp_f32_e32 v19, v7
	v_cndmask_b32_e32 v20, v134, v6, vcc
	v_lshl_add_u64 v[6:7], v[2:3], 0, s[42:43]
	v_lshl_add_u64 v[8:9], v[44:45], 0, v[8:9]
	v_lshl_add_u64 v[12:13], v[10:11], 0, s[42:43]
	global_load_ushort v139, v[2:3], off
	global_load_ushort v165, v[2:3], off offset:2048
	global_load_ushort v141, v[6:7], off
	global_load_ushort v175, v[8:9], off offset:2048
	global_load_ushort v144, v[10:11], off
	global_load_ushort v161, v[10:11], off offset:2048
	global_load_ushort v145, v[12:13], off
	global_load_ushort v172, v[14:15], off offset:2048
	v_cndmask_b32_e64 v2, v81, v80, s[18:19]
	v_cndmask_b32_e64 v10, v85, v84, s[18:19]
	v_mul_u32_u24_e32 v2, 0x2040, v2
	v_mul_u32_u24_e32 v10, 0x2040, v10
	v_lshlrev_b32_e32 v2, 1, v2
	v_mov_b32_e32 v3, v4
	v_cndmask_b32_e64 v8, v83, v82, s[18:19]
	v_lshlrev_b32_e32 v10, 1, v10
	v_mov_b32_e32 v11, v4
	v_cndmask_b32_e64 v14, v87, v86, s[18:19]
	v_lshl_add_u64 v[2:3], v[44:45], 0, v[2:3]
	v_mul_u32_u24_e32 v8, 0x4080, v8
	v_mov_b32_e32 v9, v4
	v_lshl_add_u64 v[10:11], v[44:45], 0, v[10:11]
	v_mul_u32_u24_e32 v14, 0x4080, v14
	v_mov_b32_e32 v15, v4
	v_lshl_add_u64 v[6:7], v[2:3], 0, s[42:43]
	v_lshl_add_u64 v[8:9], v[44:45], 0, v[8:9]
	v_lshl_add_u64 v[12:13], v[10:11], 0, s[42:43]
	v_lshl_add_u64 v[14:15], v[44:45], 0, v[14:15]
	global_load_ushort v149, v[2:3], off
	global_load_ushort v163, v[2:3], off offset:2048
	global_load_ushort v151, v[6:7], off
	global_load_ushort v177, v[8:9], off offset:2048
	global_load_ushort v153, v[10:11], off
	global_load_ushort v166, v[10:11], off offset:2048
; #define LAS __attribute__((address_space(3)))
; __device__ __forceinline__ float bf2f(bf16_t v) { return __uint_as_float((unsigned)v << 16); }
; __device__ __forceinline__ void hgrn_mfma(const Params& p, LAS unsigned char* lds) {
;     ...
;         float lb; { const float l0 = lbl[h * 128 + d], l1 = lbl[1024 + h * 128 + d], l2 = lbl[2048 + h * 128 + d];
;             const float mx = fmaxf(l0, fmaxf(l1, l2)); const float e0 = expf(l0 - mx), e1 = expf(l1 - mx), e2 = expf(l2 - mx); lb = e0 / (e0 + e1 + e2); }
;         f32x4 S[8];
; #pragma unroll
;         for (int mi = 0; mi < 8; ++mi) S[mi] = (f32x4){0.f, 0.f, 0.f, 0.f};
;         const bf16_t* pb = proj + (size_t)b * T * LD0 + h * 128 + d;
;         const int zoff = dir ? 3072 : 2048;
;         bf16_t rq[8], rz[8], rv[8], rp[8];
;     ...
;         HG_LOAD(0);
;         for (int n = 0; n < T / 32; ++n) {
;             LAS unsigned char* set = lds + (n & 1) * SET_BYTES;
;             LAS unsigned char* QG = set; LAS unsigned char* KG = set + 8192; LAS unsigned char* KDT = set + 16384; LAS float* DEC = (LAS float*)(set + 24576);
;             float qv[8], fv[8], vv[8], vp[8];
; #pragma unroll
;             for (int i = 0; i < 8; ++i) { qv[i] = bf2f(rq[i]); vv[i] = bf2f(rv[i]); fv[i] = bf2f(rz[i]); vp[i] = bf2f(rp[i]); }
;             if (n + 1 < T / 32) HG_LOAD(n + 1);
	global_load_ushort v154, v[12:13], off
	global_load_ushort v176, v[14:15], off offset:2048
	v_cndmask_b32_e64 v2, v89, v88, s[18:19]
	v_cndmask_b32_e64 v10, v93, v92, s[18:19]
	v_mul_u32_u24_e32 v2, 0x2040, v2
	v_mul_u32_u24_e32 v10, 0x2040, v10
	v_lshlrev_b32_e32 v2, 1, v2
	v_mov_b32_e32 v3, v4
	v_cndmask_b32_e64 v8, v91, v90, s[18:19]
	v_lshlrev_b32_e32 v10, 1, v10
	v_mov_b32_e32 v11, v4
	v_cndmask_b32_e64 v14, v95, v94, s[18:19]
	v_lshl_add_u64 v[2:3], v[44:45], 0, v[2:3]
	v_mul_u32_u24_e32 v8, 0x4080, v8
	v_mov_b32_e32 v9, v4
	v_lshl_add_u64 v[10:11], v[44:45], 0, v[10:11]
	v_mul_u32_u24_e32 v14, 0x4080, v14
	v_mov_b32_e32 v15, v4
	v_lshl_add_u64 v[6:7], v[2:3], 0, s[42:43]
	v_lshl_add_u64 v[8:9], v[44:45], 0, v[8:9]
	v_lshl_add_u64 v[12:13], v[10:11], 0, s[42:43]
	v_lshl_add_u64 v[14:15], v[44:45], 0, v[14:15]
	global_load_ushort v155, v[2:3], off
	global_load_ushort v162, v[2:3], off offset:2048
	global_load_ushort v156, v[6:7], off
	global_load_ushort v180, v[8:9], off offset:2048
	global_load_ushort v157, v[10:11], off
	global_load_ushort v164, v[10:11], off offset:2048
	global_load_ushort v158, v[12:13], off
	global_load_ushort v181, v[14:15], off offset:2048
	v_ldexp_f32 v2, v19, v17
	v_cmp_ngt_f32_e32 vcc, s48, v16
	v_add_f32_e32 v3, v0, v20
	s_add_u32 s42, s38, s46
	v_cndmask_b32_e32 v2, 0, v2, vcc
	v_cmp_nlt_f32_e32 vcc, s49, v16
	s_addc_u32 s46, s39, s47
	s_lshl_b32 s47, s54, 25
	v_cndmask_b32_e32 v2, v134, v2, vcc
	v_add_f32_e32 v2, v2, v3
	v_div_scale_f32 v3, s[58:59], v2, v2, v0
	v_rcp_f32_e32 v6, v3
	s_add_u32 s42, s42, s47
	s_addc_u32 s46, s46, 0
	s_add_u32 s42, s42, s56
	v_fma_f32 v7, -v3, v6, 1.0
	v_fmac_f32_e32 v6, v7, v6
	v_div_scale_f32 v7, vcc, v0, v2, v0
	v_mul_f32_e32 v8, v7, v6
	v_fma_f32 v9, -v3, v8, v7
	v_fmac_f32_e32 v8, v9, v6
	v_fma_f32 v3, -v3, v8, v7
	v_div_fmas_f32 v3, v3, v6, v8
	s_addc_u32 s47, s46, 0
	v_div_fixup_f32 v50, v3, v2, v0
	s_add_u32 s46, s42, s44
	v_sub_f32_e32 v52, 1.0, v50
	s_addc_u32 s47, s47, s45
	v_lshlrev_b32_e32 v2, 1, v40
	v_mov_b32_e32 v3, v4
	v_lshl_add_u64 v[42:43], s[46:47], 0, v[2:3]
	v_mov_b32_e32 v54, v50
	v_mov_b32_e32 v46, v50
	v_mov_b32_e32 v47, v50
	v_mov_b32_e32 v48, v52
	v_mov_b32_e32 v49, v52
	s_lshl_b32 s42, s55, 1
	s_mov_b32 s54, s43
	s_mov_b32 s55, s43
	s_mov_b32 s56, s43
	v_mov_b32_e32 v14, v4
	v_mov_b32_e32 v15, v4
	v_mov_b32_e32 v16, v4
	v_mov_b32_e32 v17, v4
	v_mov_b32_e32 v6, v4
	v_mov_b32_e32 v7, v4
	v_mov_b32_e32 v8, v4
	v_mov_b32_e32 v9, v4
	v_mov_b32_e32 v10, v4
	v_mov_b32_e32 v11, v4
	v_mov_b32_e32 v12, v4
	v_mov_b32_e32 v13, v4
	v_mov_b32_e32 v18, v4
	v_mov_b32_e32 v19, v4
	v_mov_b32_e32 v20, v4
	v_readfirstlane_b32 s80, v44
	v_readfirstlane_b32 s81, v45
	s_mov_b32 s84, 0x81000
	s_mov_b32 s85, 0x4080
	s_mov_b32 s86, 0x40800
	s_cmp_lg_u64 s[18:19], 0
	s_cselect_b32 s84, s84, 0xfff7f000
	s_cselect_b32 s85, s85, 0xffffbf80
	s_cselect_b32 s86, s86, 0xfffbf800
	s_nop 1
	s_add_u32 s82, s80, s42
	s_addc_u32 s83, s81, s43
	v_subrev_u32_e32 v240, s80, v44
	v_add_u32_e32 v250, 32, v41
	v_sub_u32_e32 v251, 0x7df, v41
	v_cndmask_b32_e64 v250, v251, v250, s[18:19]
	v_mul_u32_u24_e32 v250, 0x4080, v250
	v_add_u32_e32 v232, v250, v240
	v_add_u32_e32 v233, s85, v232
	v_add_u32_e32 v234, s85, v233
	v_add_u32_e32 v235, s85, v234
	v_add_u32_e32 v236, s85, v235
	v_add_u32_e32 v237, s85, v236
	v_add_u32_e32 v238, s85, v237
	v_add_u32_e32 v239, s85, v238
	v_add_u32_e32 v252, 32, v40
	v_sub_u32_e32 v253, 0x7df, v40
	v_cndmask_b32_e64 v252, v253, v252, s[18:19]
	v_mul_u32_u24_e32 v252, 0x4080, v252
	v_add_u32_e32 v242, v252, v240
	v_add_u32_e32 v243, s85, v242
	v_add_u32_e32 v244, s85, v243
	v_add_u32_e32 v245, s85, v244
	v_add_u32_e32 v246, s86, v242
	v_add_u32_e32 v247, s85, v246
	v_add_u32_e32 v248, s85, v247
	v_add_u32_e32 v249, s85, v248
	s_nop 3
.LBB0_275:
	s_bitcmp1_b32 s56, 0
	s_waitcnt vmcnt(31)
	v_lshlrev_b32_e32 v0, 16, v135
	s_waitcnt vmcnt(25)
	v_lshlrev_b32_e32 v53, 16, v138
	s_waitcnt vmcnt(1)
	v_lshlrev_b32_e32 v199, 16, v158
	s_cselect_b32 s46, 0x6200, 0
	s_add_i32 s57, s46, 0
	v_lshlrev_b32_e32 v193, 16, v139
	v_lshlrev_b32_e32 v55, 16, v141
	v_lshlrev_b32_e32 v51, 16, v137
	v_lshlrev_b32_e32 v192, 16, v136
	v_lshlrev_b32_e32 v194, 16, v144
	v_lshlrev_b32_e32 v195, 16, v145
	global_load_ushort v135, v232, s[80:81]
	global_load_ushort v167, v232, s[80:81] offset:2048
	s_nop 0
	global_load_ushort v137, v232, s[82:83]
	s_nop 0
	global_load_ushort v143, v242, s[80:81] offset:2048
	global_load_ushort v136, v233, s[80:81]
	global_load_ushort v168, v233, s[80:81] offset:2048
	s_nop 0
	global_load_ushort v138, v233, s[82:83]
	global_load_ushort v140, v243, s[80:81] offset:2048
	v_lshlrev_b32_e32 v204, 16, v149
	v_lshlrev_b32_e32 v196, 16, v151
	v_lshlrev_b32_e32 v205, 16, v153
	global_load_ushort v139, v234, s[80:81]
	global_load_ushort v169, v234, s[80:81] offset:2048
	global_load_ushort v141, v234, s[82:83]
	s_nop 0
	global_load_ushort v146, v244, s[80:81] offset:2048
	s_nop 0
	global_load_ushort v144, v235, s[80:81]
	global_load_ushort v170, v235, s[80:81] offset:2048
	global_load_ushort v145, v235, s[82:83]
	global_load_ushort v142, v245, s[80:81] offset:2048
	v_mul_f32_e32 v51, 0xbfb8aa3b, v51
	v_exp_f32_e32 v51, v51
	v_mul_f32_e32 v53, 0xbfb8aa3b, v53
	v_lshlrev_b32_e32 v197, 16, v154
	v_lshlrev_b32_e32 v206, 16, v155
	v_exp_f32_e32 v53, v53
	v_lshlrev_b32_e32 v198, 16, v156
	v_lshlrev_b32_e32 v207, 16, v157
	global_load_ushort v149, v236, s[80:81]
	global_load_ushort v173, v236, s[80:81] offset:2048
	s_nop 0
	global_load_ushort v151, v236, s[82:83]
	s_nop 0
	global_load_ushort v147, v246, s[80:81] offset:2048
	s_nop 0
	global_load_ushort v153, v237, s[80:81]
; #define LAS __attribute__((address_space(3)))
; __device__ __forceinline__ float bf2f(bf16_t v) { return __uint_as_float((unsigned)v << 16); }
; __device__ __forceinline__ bf16_t f2bf(float a) { return (bf16_t)(pk2(a, 0.f) & 0xffffu); }
; __device__ __forceinline__ float frcp(float x) { return __builtin_amdgcn_rcpf(x); }
; __device__ __forceinline__ float sigm(float x) { return frcp(1.f + __expf(-x)); }
; __device__ __forceinline__ float silu(float x) { return x * frcp(1.f + __expf(-x)); }
; __device__ __forceinline__ void hgrn_mfma(const Params& p, LAS unsigned char* lds) {
;     ...
;         HG_LOAD(0);
;         for (int n = 0; n < T / 32; ++n) {
;             LAS unsigned char* set = lds + (n & 1) * SET_BYTES;
;             LAS unsigned char* QG = set; LAS unsigned char* KG = set + 8192; LAS unsigned char* KDT = set + 16384; LAS float* DEC = (LAS float*)(set + 24576);
;             float qv[8], fv[8], vv[8], vp[8];
; #pragma unroll
;             for (int i = 0; i < 8; ++i) { qv[i] = bf2f(rq[i]); vv[i] = bf2f(rv[i]); fv[i] = bf2f(rz[i]); vp[i] = bf2f(rp[i]); }
;             if (n + 1 < T / 32) HG_LOAD(n + 1);
;             float Pl[8]; float P = 1.f;
; #pragma unroll
;             for (int i = 0; i < 8; ++i) { fv[i] = lb + (1.f - lb) * sigm(fv[i]); P *= fv[i]; Pl[i] = P; }
;             const float p0 = __shfl(P, fr), p1 = __shfl(P, fr + 16), p2 = __shfl(P, fr + 32), p3 = __shfl(P, fr + 48);
;             const float pre = (fq > 0 ? p0 : 1.f) * (fq > 1 ? p1 : 1.f) * (fq > 2 ? p2 : 1.f), tot = (p0 * p1) * (p2 * p3);
;             float kd[8];
; #pragma unroll
;             for (int i = 0; i < 8; ++i) {
;                 const int c = 8 * fq + i; const float E = pre * Pl[i], rE = frcp(E), k = 1.f - fv[i];
;                 *(LAS bf16_t*)(QG + rm_byte(c, d)) = f2bf(silu(qv[i]) * E);
;                 *(LAS bf16_t*)(KG + rm_byte(c, d)) = f2bf(k * rE);
;                 kd[i] = k * tot * rE;
;             }
	global_load_ushort v174, v237, s[80:81] offset:2048
	s_nop 0
	global_load_ushort v154, v237, s[82:83]
	global_load_ushort v148, v247, s[80:81] offset:2048
	v_add_f32_e32 v51, 1.0, v51
	v_rcp_f32_e32 v191, v51
	v_add_f32_e32 v51, 1.0, v53
	v_rcp_f32_e32 v190, v51
	v_mul_f32_e32 v51, 0xbfb8aa3b, v196
	v_exp_f32_e32 v51, v51
	global_load_ushort v155, v238, s[80:81]
	global_load_ushort v178, v238, s[80:81] offset:2048
	s_nop 0
	global_load_ushort v156, v238, s[82:83]
	s_nop 0
	global_load_ushort v150, v248, s[80:81] offset:2048
	global_load_ushort v157, v239, s[80:81]
	global_load_ushort v179, v239, s[80:81] offset:2048
	global_load_ushort v158, v239, s[82:83]
	global_load_ushort v152, v249, s[80:81] offset:2048
	v_add_u32_e32 v232, s84, v232
	v_add_u32_e32 v233, s84, v233
	v_add_u32_e32 v234, s84, v234
	v_add_u32_e32 v235, s84, v235
	v_add_u32_e32 v236, s84, v236
	v_add_u32_e32 v237, s84, v237
	v_add_u32_e32 v238, s84, v238
	v_add_u32_e32 v239, s84, v239
	v_add_u32_e32 v242, s84, v242
	v_add_u32_e32 v243, s84, v243
	v_add_u32_e32 v244, s84, v244
	v_add_u32_e32 v245, s84, v245
	v_add_u32_e32 v246, s84, v246
	v_add_u32_e32 v247, s84, v247
	v_add_u32_e32 v248, s84, v248
	v_add_u32_e32 v249, s84, v249
	v_mul_f32_e32 v188, 0xbfb8aa3b, v192
	v_add_f32_e32 v51, 1.0, v51
	v_exp_f32_e32 v188, v188
	v_rcp_f32_e32 v186, v51
	v_mul_f32_e32 v51, 0xbfb8aa3b, v199
	v_exp_f32_e32 v51, v51
	v_add_f32_e32 v188, 1.0, v188
	v_rcp_f32_e32 v189, v188
	v_mul_f32_e32 v2, 0xbfb8aa3b, v55
	v_add_f32_e32 v51, 1.0, v51
	v_mul_f32_e32 v3, 0xbfb8aa3b, v195
	v_rcp_f32_e32 v188, v51
	v_mul_f32_e32 v51, 0xbfb8aa3b, v193
	v_exp_f32_e32 v2, v2
	v_exp_f32_e32 v3, v3
	v_exp_f32_e32 v51, v51
	v_mul_f32_e32 v208, v189, v192
	v_mul_f32_e32 v189, 0xbfb8aa3b, v194
	v_exp_f32_e32 v189, v189
	v_add_f32_e32 v2, 1.0, v2
	v_add_f32_e32 v3, 1.0, v3
	v_add_f32_e32 v51, 1.0, v51
	v_rcp_f32_e32 v2, v2
	v_rcp_f32_e32 v3, v3
	v_mul_f32_e32 v53, 0xbfb8aa3b, v197
	v_rcp_f32_e32 v51, v51
	v_exp_f32_e32 v53, v53
	v_mul_f32_e32 v55, 0xbfb8aa3b, v198
	v_add_f32_e32 v189, 1.0, v189
	v_exp_f32_e32 v55, v55
	v_rcp_f32_e32 v189, v189
	v_pk_fma_f32 v[182:183], v[48:49], v[190:191], v[46:47]
	v_mul_f32_e32 v210, v51, v193
	v_pk_mul_f32 v[184:185], v[182:183], v[182:183] op_sel:[0,1] op_sel_hi:[1,0]
	v_pk_fma_f32 v[192:193], v[48:49], v[2:3], v[46:47]
	v_add_f32_e32 v53, 1.0, v53
	v_mov_b32_e32 v187, v184
	v_mov_b32_e32 v2, v52
	v_mov_b32_e32 v3, v192
	v_rcp_f32_e32 v53, v53
	v_add_f32_e32 v55, 1.0, v55
	v_mul_f32_e32 v212, v189, v194
	v_pk_mul_f32 v[194:195], v[2:3], v[186:187]
	v_mov_b32_e32 v51, v193
	v_rcp_f32_e32 v55, v55
	v_pk_fma_f32 v[186:187], v[2:3], v[186:187], v[50:51]
	v_pk_mul_f32 v[196:197], v[50:51], v[194:195]
	v_fma_f32 v53, v52, v53, v50
	v_mov_b32_e32 v187, v197
	v_pk_mul_f32 v[198:199], v[186:187], v[196:197] op_sel:[0,1] op_sel_hi:[1,0]
	v_fma_f32 v55, v52, v55, v50
	v_mov_b32_e32 v189, v198
	v_pk_mul_f32 v[200:201], v[52:53], v[188:189]
	v_mul_f32_e32 v185, 0xbfb8aa3b, v0
	v_pk_fma_f32 v[188:189], v[52:53], v[188:189], v[54:55]
	v_mul_f32_e32 v51, v55, v201
	v_exp_f32_e32 v185, v185
	v_mul_f32_e32 v189, v188, v51
	ds_bpermute_b32 v2, v56, v189
	ds_bpermute_b32 v202, v57, v189
	ds_bpermute_b32 v3, v58, v189
	v_add_f32_e32 v185, 1.0, v185
	v_rcp_f32_e32 v185, v185
	v_pk_add_f32 v[190:191], v[182:183], 1.0 op_sel_hi:[1,0] neg_lo:[1,0] neg_hi:[1,0]
	s_waitcnt lgkmcnt(2)
	v_cndmask_b32_e64 v182, v2, 1.0, s[4:5]
	s_waitcnt lgkmcnt(1)
	v_cndmask_b32_e64 v194, 1.0, v202, s[6:7]
	v_mul_f32_e32 v182, v182, v194
	s_waitcnt lgkmcnt(0)
	v_cndmask_b32_e64 v194, 1.0, v3, s[8:9]
	v_mul_f32_e32 v194, v182, v194
	v_mul_f32_e32 v0, v185, v0
	v_mul_f32_e32 v182, v183, v194
	v_mul_f32_e32 v0, v0, v182
	v_add_u32_e32 v185, s57, v97
	ds_bpermute_b32 v203, v59, v189
	v_rcp_f32_e32 v183, v182
	v_cvt_pk_bf16_f32 v0, v0, s0
	ds_write_b16 v185, v0
	v_mul_f32_e32 v0, v184, v194
	v_rcp_f32_e32 v182, v0
	v_mul_f32_e32 v0, v208, v0
	v_mul_f32_e32 v184, v191, v183
	v_add_u32_e32 v209, s57, v125
	s_waitcnt lgkmcnt(1)
	v_pk_mul_f32 v[2:3], v[2:3], v[202:203]
	v_cvt_pk_bf16_f32 v0, v0, s0
	v_cvt_pk_bf16_f32 v184, v184, s0
	v_pk_mul_f32 v[2:3], v[2:3], v[2:3] op_sel:[0,1] op_sel_hi:[1,0]
	ds_write_b16 v185, v184 offset:8192
	ds_write_b16 v209, v0 offset:256
	v_mul_f32_e32 v0, v190, v182
	v_pk_mul_f32 v[184:185], v[190:191], v[2:3] op_sel_hi:[1,0]
	v_cvt_pk_bf16_f32 v0, v0, s0
	v_pk_mul_f32 v[184:185], v[182:183], v[184:185]
	ds_write_b16 v209, v0 offset:8448
	v_mul_f32_e32 v0, v195, v194
	v_mul_f32_e32 v195, v197, v194
	v_pk_mov_b32 v[182:183], v[184:185], v[184:185] op_sel:[1,0]
	v_rcp_f32_e32 v184, v0
	v_rcp_f32_e32 v185, v195
	v_mul_f32_e32 v0, v210, v0
	v_pk_add_f32 v[190:191], v[192:193], 1.0 op_sel_hi:[1,0] neg_lo:[1,0] neg_hi:[1,0]
	v_add_u32_e32 v211, s57, v126
	v_cvt_pk_bf16_f32 v0, v0, s0
	v_pk_mul_f32 v[192:193], v[190:191], v[2:3] op_sel_hi:[1,0]
	ds_write_b16 v211, v0 offset:512
	v_mul_f32_e32 v0, v190, v184
	v_pk_mul_f32 v[192:193], v[184:185], v[192:193]
	v_mul_f32_e32 v184, 0xbfb8aa3b, v204
	v_cvt_pk_bf16_f32 v0, v0, s0
	v_exp_f32_e32 v184, v184
	ds_write_b16 v211, v0 offset:8704
	v_mul_f32_e32 v0, v212, v195
	v_add_u32_e32 v187, s57, v127
	v_cvt_pk_bf16_f32 v0, v0, s0
	ds_write_b16 v187, v0 offset:768
	v_mul_f32_e32 v0, v191, v185
	v_cvt_pk_bf16_f32 v0, v0, s0
	v_add_f32_e32 v184, 1.0, v184
	v_rcp_f32_e32 v185, v184
	ds_write_b16 v187, v0 offset:8960
	v_mul_f32_e32 v187, 0xbfb8aa3b, v205
	v_exp_f32_e32 v187, v187
	v_mul_f32_e32 v0, v198, v194
	v_mul_f32_e32 v185, v185, v204
	v_rcp_f32_e32 v184, v0
	v_mul_f32_e32 v0, v185, v0
	v_add_f32_e32 v185, 1.0, v187
	v_rcp_f32_e32 v187, v185
	v_cvt_pk_bf16_f32 v0, v0, s0
; __device__ __forceinline__ void hgrn_mfma(const Params& p, LAS unsigned char* lds) {
;     ...
;             for (int i = 0; i < 8; ++i) {
;                 const int c = 8 * fq + i; const float E = pre * Pl[i], rE = frcp(E), k = 1.f - fv[i];
;                 *(LAS bf16_t*)(QG + rm_byte(c, d)) = f2bf(silu(qv[i]) * E);
;                 *(LAS bf16_t*)(KG + rm_byte(c, d)) = f2bf(k * rE);
;                 kd[i] = k * tot * rE;
;             }
;             { u32x4 wv; wv.x = pk2(kd[0], kd[1]); wv.y = pk2(kd[2], kd[3]); wv.z = pk2(kd[4], kd[5]); wv.w = pk2(kd[6], kd[7]);
;               *(LAS u32x4*)(KDT + d * 64 + ((fq ^ ((d >> 2) & 3)) << 4)) = wv; }
;             if (fq == 0) DEC[d] = tot;
;             const bf16x8 vB = pack8((f32x4){vv[0], vv[1], vv[2], vv[3]}, (f32x4){vv[4], vv[5], vv[6], vv[7]});
;             const bf16x8 vP = pack8((f32x4){vp[0], vp[1], vp[2], vp[3]}, (f32x4){vp[4], vp[5], vp[6], vp[7]});
;             __syncthreads();
;             f32x4 at00 = {0.f, 0.f, 0.f, 0.f}, at01 = at00, at11 = at00;
; #pragma unroll
;             for (int ks = 0; ks < 4; ++ks) {
;                 const int d0 = 32 * ks + 8 * fq;
;                 const bf16x8 kg0 = *(const LAS bf16x8*)(KG + rm_byte(fr, d0)), kg1 = *(const LAS bf16x8*)(KG + rm_byte(16 + fr, d0));
;                 const bf16x8 qg0 = *(const LAS bf16x8*)(QG + rm_byte(fr, d0)), qg1 = *(const LAS bf16x8*)(QG + rm_byte(16 + fr, d0));
;                 at00 = __builtin_amdgcn_mfma_f32_16x16x32_bf16(kg0, qg0, at00, 0, 0, 0);
;                 at01 = __builtin_amdgcn_mfma_f32_16x16x32_bf16(kg0, qg1, at01, 0, 0, 0);
;                 at11 = __builtin_amdgcn_mfma_f32_16x16x32_bf16(kg1, qg1, at11, 0, 0, 0);
;             }
; #pragma unroll
;             for (int j = 0; j < 4; ++j) { const bool ok = (4 * fq + j) <= fr; at00[j] = ok ? at00[j] : 0.f; at11[j] = ok ? at11[j] : 0.f; }
;             const bf16x8 bi0 = pack8(at00, (f32x4){0.f, 0.f, 0.f, 0.f}), bi1 = pack8(at01, at11);
;             f32x4 o0 = {0.f, 0.f, 0.f, 0.f}, o1 = o0;
;             o0 = __builtin_amdgcn_mfma_f32_16x16x32_bf16(vP, bi0, o0, 0, 0, 0);
;             o1 = __builtin_amdgcn_mfma_f32_16x16x32_bf16(vP, bi1, o1, 0, 0, 0);
; #pragma unroll
;             for (int ks = 0; ks < 4; ++ks) {
;                 const bf16x8 sb = pack8(S[2 * ks], S[2 * ks + 1]);
;                 const int da = 32 * ks + 4 * fq, db = da + 16;
	v_add_u32_e32 v190, s57, v128
	ds_write_b16 v190, v0 offset:1024
	v_mul_f32_e32 v0, v201, v194
	v_mul_f32_e32 v187, v187, v205
	v_rcp_f32_e32 v185, v0
	v_mul_f32_e32 v0, v187, v0
	v_mov_b32_e32 v187, v53
	v_pk_add_f32 v[186:187], v[186:187], 1.0 op_sel_hi:[1,0] neg_lo:[1,0] neg_hi:[1,0]
	v_cvt_pk_bf16_f32 v0, v0, s0
	v_mul_f32_e32 v53, v186, v184
	v_cvt_pk_bf16_f32 v53, v53, s0
	ds_write_b16 v190, v53 offset:9216
	v_mul_f32_e32 v53, 0xbfb8aa3b, v206
	v_exp_f32_e32 v53, v53
	v_add_u32_e32 v195, s57, v129
	ds_write_b16 v195, v0 offset:1280
	v_mul_f32_e32 v0, v187, v185
	v_add_f32_e32 v53, 1.0, v53
	v_rcp_f32_e32 v53, v53
	v_cvt_pk_bf16_f32 v0, v0, s0
	ds_write_b16 v195, v0 offset:9472
	v_mul_f32_e32 v0, v51, v194
	v_mul_f32_e32 v51, v53, v206
	v_mul_f32_e32 v53, 0xbfb8aa3b, v207
	v_exp_f32_e32 v53, v53
	v_pk_mul_f32 v[190:191], v[186:187], v[2:3] op_sel_hi:[1,0]
	v_mov_b32_e32 v186, v55
	v_pk_mul_f32 v[190:191], v[184:185], v[190:191]
	v_add_f32_e32 v53, 1.0, v53
	v_rcp_f32_e32 v184, v0
	v_mul_f32_e32 v0, v51, v0
	v_rcp_f32_e32 v53, v53
	v_cvt_pk_bf16_f32 v0, v0, s0
	v_add_u32_e32 v51, s57, v130
	ds_write_b16 v51, v0 offset:1536
	v_mul_f32_e32 v0, v189, v194
	v_rcp_f32_e32 v185, v0
	v_mov_b32_e32 v187, v188
	v_mul_f32_e32 v53, v53, v207
	v_pk_add_f32 v[186:187], v[186:187], 1.0 op_sel_hi:[1,0] neg_lo:[1,0] neg_hi:[1,0]
	v_mul_f32_e32 v0, v53, v0
	v_mul_f32_e32 v55, v186, v184
	v_cvt_pk_bf16_f32 v0, v0, s0
	v_add_u32_e32 v53, s57, v131
	v_cvt_pk_bf16_f32 v55, v55, s0
	ds_write_b16 v51, v55 offset:9728
	v_pk_mul_f32 v[188:189], v[186:187], v[2:3] op_sel_hi:[1,0]
	ds_write_b16 v53, v0 offset:1792
	v_mul_f32_e32 v0, v187, v185
	v_pk_mul_f32 v[188:189], v[184:185], v[188:189]
	v_cvt_pk_bf16_f32 v0, v0, s0
	v_add_u32_e32 v3, s57, v60
	ds_write_b16 v53, v0 offset:9984
	v_cvt_pk_bf16_f32 v182, v182, v183
	v_cvt_pk_bf16_f32 v183, v192, v193
	v_cvt_pk_bf16_f32 v184, v190, v191
	v_cvt_pk_bf16_f32 v185, v188, v189
	v_add_u32_e32 v0, v3, v61
	ds_write_b128 v0, v[182:185] offset:16384
	s_and_saveexec_b64 s[46:47], s[4:5]
	v_add_u32_e32 v0, v3, v118
	ds_write_b32 v0, v2 offset:24576
	s_or_b64 exec, exec, s[46:47]
	v_add_u32_e32 v2, s57, v98
	s_waitcnt lgkmcnt(0)
	s_barrier
	ds_read_b128 v[182:185], v2 offset:8192
	v_lshlrev_b32_e32 v3, 16, v5
	v_add_u32_e32 v5, s57, v99
	ds_read_b128 v[186:189], v5 offset:8192
	ds_read_b128 v[190:193], v2
	ds_read_b128 v[194:197], v5
	v_add_u32_e32 v5, s57, v100
	ds_read_b128 v[198:201], v5 offset:8192
	v_add_u32_e32 v51, s57, v101
	ds_read_b128 v[202:205], v51 offset:8192
	ds_read_b128 v[206:209], v5
	v_add_u32_e32 v5, s57, v102
	s_waitcnt lgkmcnt(4)
	v_mfma_f32_16x16x32_bf16 v[190:193], v[182:185], v[190:193], 0
	ds_read_b128 v[210:213], v51
	ds_read_b128 v[214:217], v5 offset:8192
	v_add_u32_e32 v51, s57, v103
	s_waitcnt lgkmcnt(5)
	v_mfma_f32_16x16x32_bf16 v[186:189], v[186:189], v[194:197], 0
	v_lshlrev_b32_e32 v0, 16, v171
	v_lshlrev_b32_e32 v55, 16, v180
	s_waitcnt vmcnt(32)
	v_lshlrev_b32_e32 v171, 16, v181
	s_waitcnt lgkmcnt(2)
	v_mfma_f32_16x16x32_bf16 v[190:193], v[198:201], v[206:209], v[190:193]
	ds_read_b128 v[206:209], v51 offset:8192
	ds_read_b128 v[218:221], v5
	v_add_u32_e32 v5, s57, v104
	ds_read_b128 v[224:227], v5 offset:8192
	s_waitcnt lgkmcnt(4)
	v_mfma_f32_16x16x32_bf16 v[186:189], v[202:205], v[210:213], v[186:189]
	ds_read_b128 v[202:205], v51
	v_add_u32_e32 v51, s57, v105
	v_lshlrev_b32_e32 v2, 16, v175
	v_mfma_f32_16x16x32_bf16 v[180:183], v[182:185], v[194:197], 0
	v_lshlrev_b32_e32 v53, 16, v177
	s_add_i32 s56, s56, 1
	s_waitcnt lgkmcnt(2)
	v_mfma_f32_16x16x32_bf16 v[190:193], v[214:217], v[218:221], v[190:193]
	ds_read_b128 v[218:221], v51 offset:8192
	ds_read_b128 v[228:231], v5
	v_lshlrev_b32_e32 v5, 16, v172
	s_waitcnt lgkmcnt(2)
	v_mfma_f32_16x16x32_bf16 v[186:189], v[206:209], v[202:205], v[186:189]
	ds_read_b128 v[206:209], v51
	v_lshlrev_b32_e32 v51, 16, v176
	v_mfma_f32_16x16x32_bf16 v[180:183], v[198:201], v[210:213], v[180:183]
	s_waitcnt lgkmcnt(1)
	v_mfma_f32_16x16x32_bf16 v[190:193], v[224:227], v[228:231], v[190:193]
	v_mfma_f32_16x16x32_bf16 v[180:183], v[214:217], v[202:205], v[180:183]
	s_waitcnt lgkmcnt(0)
	v_mfma_f32_16x16x32_bf16 v[186:189], v[218:221], v[206:209], v[186:189]
	v_cvt_pk_bf16_f32 v218, v0, v3
	v_cvt_pk_bf16_f32 v219, v2, v5
	v_cvt_pk_bf16_f32 v220, v53, v51
	v_cvt_pk_bf16_f32 v221, v55, v171
	s_nop 0
	v_cndmask_b32_e64 v0, v190, 0, s[10:11]
	v_cndmask_b32_e64 v2, 0, v191, s[12:13]
	v_cndmask_b32_e64 v3, v192, 0, s[14:15]
	v_cndmask_b32_e64 v5, v193, 0, s[16:17]
	v_mfma_f32_16x16x32_bf16 v[180:183], v[224:227], v[206:209], v[180:183]
	v_cvt_pk_bf16_f32 v2, v0, v2
	v_cvt_pk_bf16_f32 v3, v3, v5
	v_mov_b32_e32 v5, v4
	v_add_u32_e32 v0, s57, v62
	v_cndmask_b32_e64 v51, v186, 0, s[10:11]
	v_cndmask_b32_e64 v53, 0, v187, s[12:13]
	v_mfma_f32_16x16x32_bf16 v[184:187], v[218:221], v[2:5], 0
	v_add_u32_e32 v2, s57, v63
	v_add_u32_e32 v3, v0, v106
	v_cndmask_b32_e64 v55, v188, 0, s[14:15]
	v_cndmask_b32_e64 v171, v189, 0, s[16:17]
	v_add_u32_e32 v5, v0, v107
	ds_read_b64 v[192:193], v3
	ds_read_b64 v[194:195], v5
	v_add_u32_e32 v3, v2, v106
	v_cvt_pk_bf16_f32 v180, v180, v181
	v_cvt_pk_bf16_f32 v181, v182, v183
	v_cvt_pk_bf16_f32 v182, v51, v53
	v_cvt_pk_bf16_f32 v183, v55, v171
	v_cvt_pk_bf16_f32 v188, v34, v35
	v_cvt_pk_bf16_f32 v189, v36, v37
	v_cvt_pk_bf16_f32 v190, v30, v31
	v_cvt_pk_bf16_f32 v191, v32, v33
	v_add_u32_e32 v5, v2, v107
	ds_read_b64 v[196:197], v3
	ds_read_b64 v[198:199], v5
	v_mfma_f32_16x16x32_bf16 v[180:183], v[218:221], v[180:183], 0
	v_add_u32_e32 v53, v0, v108
	v_add_u32_e32 v55, v0, v109
	v_lshlrev_b32_e32 v5, 16, v160
	s_waitcnt lgkmcnt(2)
; #define LAS __attribute__((address_space(3)))
; __device__ __forceinline__ unsigned pk2(float a, float b) { f32x2 v = {a, b}; bf16x2_t r = __builtin_convertvector(v, bf16x2_t); return __builtin_bit_cast(unsigned, r); }
; __device__ __forceinline__ bf16x8 pack8(const f32x4& a, const f32x4& b) { u32x4 w; w.x = pk2(a.x, a.y); w.y = pk2(a.z, a.w); w.z = pk2(b.x, b.y); w.w = pk2(b.z, b.w); return __builtin_bit_cast(bf16x8, w); }
; __device__ __forceinline__ void hgrn_mfma(const Params& p, LAS unsigned char* lds) {
;     ...
;             for (int ks = 0; ks < 4; ++ks) {
;                 const bf16x8 sb = pack8(S[2 * ks], S[2 * ks + 1]);
;                 const int da = 32 * ks + 4 * fq, db = da + 16;
;                 const bf16x4 q0a = *(const LAS bf16x4*)(QG + rm_byte(fr, da)), q0b = *(const LAS bf16x4*)(QG + rm_byte(fr, db));
;                 const bf16x4 q1a = *(const LAS bf16x4*)(QG + rm_byte(16 + fr, da)), q1b = *(const LAS bf16x4*)(QG + rm_byte(16 + fr, db));
;                 const bf16x8 qp0 = {q0a[0], q0a[1], q0a[2], q0a[3], q0b[0], q0b[1], q0b[2], q0b[3]}, qp1 = {q1a[0], q1a[1], q1a[2], q1a[3], q1b[0], q1b[1], q1b[2], q1b[3]};
;                 o0 = __builtin_amdgcn_mfma_f32_16x16x32_bf16(sb, qp0, o0, 0, 0, 0);
;                 o1 = __builtin_amdgcn_mfma_f32_16x16x32_bf16(sb, qp1, o1, 0, 0, 0);
;             }
;             { const int c0 = fr, c1 = 16 + fr; const int t0 = dir ? (T - 1 - (32 * n + c0)) : (32 * n + c0), t1 = dir ? (T - 1 - (32 * n + c1)) : (32 * n + c1);
;               bf16_t* ob = oscr + ((size_t)dir * M + (size_t)b * T) * 1024 + h * 128 + 16 * w + 4 * fq;
;               u32x2 w0; w0.x = pk2(o0[0], o0[1]); w0.y = pk2(o0[2], o0[3]); u32x2 w1; w1.x = pk2(o1[0], o1[1]); w1.y = pk2(o1[2], o1[3]);
;               *(u32x2*)(ob + (size_t)t0 * 1024) = w0; *(u32x2*)(ob + (size_t)t1 * 1024) = w1; }
; #pragma unroll
;             for (int mi = 0; mi < 8; ++mi) {
;                 const int dr = 16 * mi + fr;
;                 const bf16x8 ka = *(const LAS bf16x8*)(KDT + dr * 64 + ((fq ^ ((dr >> 2) & 3)) << 4));
;                 const f32x4 dc = *(const LAS f32x4*)(DEC + 16 * mi + 4 * fq);
;                 S[mi] = __builtin_amdgcn_mfma_f32_16x16x32_bf16(ka, vB, S[mi] * dc, 0, 0, 0);
;             }
	v_mfma_f32_16x16x32_bf16 v[184:187], v[188:191], v[192:195], v[184:187]
	ds_read_b64 v[192:193], v53
	ds_read_b64 v[194:195], v55
	v_add_u32_e32 v53, v2, v108
	v_add_u32_e32 v55, v2, v109
	s_waitcnt lgkmcnt(2)
	v_mfma_f32_16x16x32_bf16 v[180:183], v[188:191], v[196:199], v[180:183]
	v_cvt_pk_bf16_f32 v188, v26, v27
	v_cvt_pk_bf16_f32 v189, v28, v29
	v_cvt_pk_bf16_f32 v190, v22, v23
	v_cvt_pk_bf16_f32 v191, v24, v25
	ds_read_b64 v[196:197], v53
	ds_read_b64 v[198:199], v55
	v_add_u32_e32 v160, v0, v110
	s_waitcnt lgkmcnt(2)
	v_mfma_f32_16x16x32_bf16 v[184:187], v[188:191], v[192:195], v[184:187]
	v_lshlrev_b32_e32 v53, 16, v161
	v_add_u32_e32 v161, v0, v111
	ds_read_b64 v[192:193], v160
	ds_read_b64 v[194:195], v161
	v_add_u32_e32 v160, v2, v110
	s_waitcnt lgkmcnt(2)
	v_mfma_f32_16x16x32_bf16 v[180:183], v[188:191], v[196:199], v[180:183]
	v_cvt_pk_bf16_f32 v188, v18, v19
	v_cvt_pk_bf16_f32 v189, v20, v21
	v_cvt_pk_bf16_f32 v190, v10, v11
	v_cvt_pk_bf16_f32 v191, v12, v13
	v_add_u32_e32 v161, v2, v111
	ds_read_b64 v[196:197], v160
	ds_read_b64 v[198:199], v161
	v_lshlrev_b32_e32 v3, 16, v159
	v_cvt_pk_bf16_f32 v160, v3, v5
	v_add_u32_e32 v3, v0, v112
	v_lshlrev_b32_e32 v51, 16, v165
	v_lshlrev_b32_e32 v55, 16, v163
	v_lshlrev_b32_e32 v159, 16, v166
	s_waitcnt lgkmcnt(2)
	v_mfma_f32_16x16x32_bf16 v[184:187], v[188:191], v[192:195], v[184:187]
	v_lshlrev_b32_e32 v166, 16, v162
	v_lshlrev_b32_e32 v171, 16, v164
	v_add_u32_e32 v0, v0, v113
	s_waitcnt lgkmcnt(0)
	v_mfma_f32_16x16x32_bf16 v[180:183], v[188:191], v[196:199], v[180:183]
	v_cvt_pk_bf16_f32 v188, v6, v7
	v_cvt_pk_bf16_f32 v189, v8, v9
	v_cvt_pk_bf16_f32 v190, v14, v15
	v_cvt_pk_bf16_f32 v191, v16, v17
	ds_read_b64 v[162:163], v3
	ds_read_b64 v[164:165], v0
	v_add_u32_e32 v0, v2, v112
	v_add_u32_e32 v2, v2, v113
	ds_read_b64 v[192:193], v0
	ds_read_b64 v[194:195], v2
	s_waitcnt lgkmcnt(2)
	v_mfma_f32_16x16x32_bf16 v[184:187], v[188:191], v[162:165], v[184:187]
	v_add_u32_e32 v0, s54, v64
	v_add_u32_e32 v3, s55, v1
	v_cndmask_b32_e64 v2, v0, v3, s[18:19]
	v_add_u32_e32 v0, s54, v65
	v_add_u32_e32 v3, 16, v3
	s_waitcnt lgkmcnt(0)
	v_mfma_f32_16x16x32_bf16 v[180:183], v[188:191], v[192:195], v[180:183]
	v_cndmask_b32_e64 v164, v0, v3, s[18:19]
	v_ashrrev_i32_e32 v3, 31, v2
	v_lshlrev_b64 v[2:3], 11, v[2:3]
	v_cvt_pk_bf16_f32 v176, v184, v185
	v_cvt_pk_bf16_f32 v177, v186, v187
	v_lshl_add_u64 v[2:3], v[42:43], 0, v[2:3]
	v_add_u32_e32 v0, s57, v61
	v_cvt_pk_bf16_f32 v161, v51, v53
	global_store_dwordx2 v[2:3], v[176:177], off
	v_lshl_add_u32 v5, v40, 2, s57
	v_add_u32_e32 v53, v0, v114
	v_cvt_pk_bf16_f32 v204, v180, v181
	v_cvt_pk_bf16_f32 v205, v182, v183
	v_add_u32_e32 v51, v0, v96
	ds_read_b128 v[180:183], v5 offset:24576
	ds_read_b128 v[184:187], v51 offset:16384
	ds_read_b128 v[192:195], v53 offset:16384
	ds_read_b128 v[188:191], v5 offset:24640
	v_cvt_pk_bf16_f32 v162, v55, v159
	v_cvt_pk_bf16_f32 v163, v166, v171
	s_waitcnt lgkmcnt(3)
	v_pk_mul_f32 v[36:37], v[36:37], v[182:183]
	v_pk_mul_f32 v[34:35], v[34:35], v[180:181]
	ds_read_b128 v[180:183], v51 offset:20480
	s_waitcnt lgkmcnt(1)
	v_pk_mul_f32 v[32:33], v[32:33], v[190:191]
	v_pk_mul_f32 v[30:31], v[30:31], v[188:189]
	v_add_u32_e32 v53, v0, v115
	v_mfma_f32_16x16x32_bf16 v[34:37], v[184:187], v[160:163], v[34:37]
	ds_read_b128 v[184:187], v53 offset:16384
	ds_read_b128 v[188:191], v51 offset:23552
	v_add_u32_e32 v0, v0, v116
	v_ashrrev_i32_e32 v165, 31, v164
	v_mfma_f32_16x16x32_bf16 v[30:33], v[192:195], v[160:163], v[30:33]
	ds_read_b128 v[192:195], v5 offset:24704
	ds_read_b128 v[196:199], v0 offset:16384
	ds_read_b128 v[200:203], v5 offset:24768
	v_lshlrev_b64 v[2:3], 11, v[164:165]
	s_add_i32 s55, s55, 32
	s_sub_i32 s54, s54, 32
	s_waitcnt lgkmcnt(2)
	v_pk_mul_f32 v[28:29], v[28:29], v[194:195]
	v_pk_mul_f32 v[26:27], v[26:27], v[192:193]
	s_waitcnt lgkmcnt(0)
	v_pk_mul_f32 v[24:25], v[24:25], v[202:203]
	v_pk_mul_f32 v[22:23], v[22:23], v[200:201]
	v_mfma_f32_16x16x32_bf16 v[26:29], v[184:187], v[160:163], v[26:29]
	ds_read_b128 v[184:187], v5 offset:24832
	v_lshl_add_u64 v[2:3], v[42:43], 0, v[2:3]
	s_cmpk_eq_i32 s55, 0x7e0
	v_mfma_f32_16x16x32_bf16 v[22:25], v[196:199], v[160:163], v[22:25]
	ds_read_b128 v[192:195], v51 offset:21504
	ds_read_b128 v[196:199], v5 offset:24896
	s_waitcnt lgkmcnt(2)
	v_pk_mul_f32 v[20:21], v[20:21], v[186:187]
	v_pk_mul_f32 v[18:19], v[18:19], v[184:185]
	ds_read_b128 v[184:187], v5 offset:24960
	global_store_dwordx2 v[2:3], v[204:205], off
	v_mfma_f32_16x16x32_bf16 v[18:21], v[180:183], v[160:163], v[18:21]
	ds_read_b128 v[180:183], v51 offset:22528
	s_waitcnt lgkmcnt(2)
	v_pk_mul_f32 v[12:13], v[12:13], v[198:199]
	v_pk_mul_f32 v[10:11], v[10:11], v[196:197]
	s_nop 1
	v_mfma_f32_16x16x32_bf16 v[10:13], v[192:195], v[160:163], v[10:13]
	ds_read_b128 v[192:195], v5 offset:25024
	s_waitcnt lgkmcnt(2)
	v_pk_mul_f32 v[8:9], v[8:9], v[186:187]
	v_pk_mul_f32 v[6:7], v[6:7], v[184:185]
	s_waitcnt lgkmcnt(0)
	v_pk_mul_f32 v[16:17], v[16:17], v[194:195]
	v_pk_mul_f32 v[14:15], v[14:15], v[192:193]
	v_mfma_f32_16x16x32_bf16 v[6:9], v[180:183], v[160:163], v[6:9]
	s_nop 0
	v_mfma_f32_16x16x32_bf16 v[14:17], v[188:191], v[160:163], v[14:17]
	s_cbranch_scc1 .LBB0_279
	s_waitcnt vmcnt(4)
	v_mov_b32_e32 v164, v179
	v_mov_b32_e32 v162, v178
	v_mov_b32_e32 v166, v174
	v_mov_b32_e32 v163, v173
	v_mov_b32_e32 v161, v170
	v_mov_b32_e32 v165, v169
	v_mov_b32_e32 v160, v168
	v_mov_b32_e32 v159, v167
	s_waitcnt vmcnt(2)
	v_mov_b32_e32 v181, v152
	v_mov_b32_e32 v180, v150
	v_mov_b32_e32 v176, v148
	v_mov_b32_e32 v177, v147
	v_mov_b32_e32 v172, v142
	v_mov_b32_e32 v175, v146
	v_mov_b32_e32 v5, v140
	v_mov_b32_e32 v171, v143
	s_branch .LBB0_275
